# GEMM phases: tail_stagger start delays bypassed (all workgroups start their tiles immediately)
# baseline (speedup 1.0000x reference)
.LBB0_978:
	s_or_b64 exec, exec, s[0:1]
	s_mov_b64 s[6:7], s[72:73]
	s_waitcnt lgkmcnt(0)
	s_barrier
	s_load_dwordx2 s[4:5], s[6:7], 0x120
	s_load_dwordx2 s[8:9], s[6:7], 0x140
	s_load_dwordx2 s[0:1], s[6:7], 0x260
	s_load_dwordx2 s[10:11], s[6:7], 0x178
	s_and_b64 s[6:7], s[38:39], exec
	s_movk_i32 s6, 0x80
	s_cselect_b32 s25, s6, 0x88
	s_lshl_b32 s12, s25, 2
	v_readlane_b32 s7, v255, 27
	s_mul_hi_u32 s7, s12, s7
	v_readlane_b32 s14, v255, 28
	s_mul_i32 s7, s7, s14
	s_sub_i32 s7, s12, s7
	s_sub_i32 s13, s7, s14
	s_cmp_ge_u32 s7, s14
	s_cselect_b32 s7, s13, s7
	s_sub_i32 s13, s7, s14
	s_cmp_ge_u32 s7, s14
	s_cselect_b32 s7, s13, s7
	s_mov_b32 s26, s2
	s_mov_b32 s6, s2
	s_cmp_eq_u32 s7, 0
	s_cselect_b64 s[14:15], -1, 0
	s_cmp_lt_i32 s6, s7
	s_cselect_b64 s[16:17], -1, 0
	s_or_b64 s[14:15], s[14:15], s[16:17]
	s_and_b64 vcc, exec, s[14:15]
	s_branch .LBB0_981
	s_sub_i32 s6, s6, s7
	s_and_b32 s6, s6, 3
	s_mul_i32 s13, s6, 0x1068
	s_memrealtime s[6:7]
	s_memrealtime s[14:15]
	s_addk_i32 s13, 0x1068
	s_waitcnt lgkmcnt(0)
	s_and_b32 s7, s13, 0x7ff8
	s_mulk_i32 s7, 0x6667
	s_lshr_b32 s7, s7, 19
	s_sub_i32 s13, s14, s6
	s_cmp_le_u32 s7, s13
	s_cbranch_scc1 .LBB0_981

.LBB0_1222:
	s_or_b64 exec, exec, s[0:1]
	s_mov_b64 s[0:1], s[72:73]
	s_waitcnt lgkmcnt(0)
	s_barrier
	s_load_dwordx2 s[10:11], s[0:1], 0x130
	s_load_dwordx2 s[12:13], s[0:1], 0x268
	s_load_dwordx2 s[14:15], s[0:1], 0x230
	s_load_dwordx2 s[16:17], s[0:1], 0x248
	s_and_b64 s[0:1], s[38:39], exec
	s_movk_i32 s0, 0x110
	s_cselect_b32 s28, 0x100, s0
	s_lshl_b32 s18, s28, 3
	v_readlane_b32 s1, v255, 27
	s_mul_hi_u32 s1, s18, s1
	v_readlane_b32 s5, v255, 28
	s_mul_i32 s1, s1, s5
	s_sub_i32 s1, s18, s1
	s_sub_i32 s4, s1, s5
	s_cmp_ge_u32 s1, s5
	s_cselect_b32 s1, s4, s1
	s_sub_i32 s4, s1, s5
	s_cmp_ge_u32 s1, s5
	s_cselect_b32 s1, s4, s1
	s_mov_b32 s26, s2
	s_mov_b32 s0, s2
	s_cmp_eq_u32 s1, 0
	s_cselect_b64 s[4:5], -1, 0
	s_cmp_lt_i32 s0, s1
	s_cselect_b64 s[6:7], -1, 0
	s_or_b64 s[4:5], s[4:5], s[6:7]
	s_and_b64 vcc, exec, s[4:5]
	s_branch .LBB0_1225
	s_sub_i32 s0, s0, s1
	s_and_b32 s0, s0, 3
	s_mul_i32 s6, s0, 0x20d0
	s_memrealtime s[0:1]
	s_memrealtime s[4:5]
	s_addk_i32 s6, 0x20d0
	s_waitcnt lgkmcnt(0)
	s_and_b32 s1, s6, 0xfff0
	s_mul_i32 s1, s1, 0xcccd
	s_lshr_b32 s1, s1, 20
	s_sub_i32 s4, s4, s0
	s_cmp_le_u32 s1, s4
	s_cbranch_scc1 .LBB0_1225

.LBB0_1307:
	s_or_b64 exec, exec, s[0:1]
	s_mov_b64 s[0:1], s[72:73]
	s_waitcnt lgkmcnt(0)
	s_barrier
	s_load_dwordx2 s[12:13], s[0:1], 0x238
	s_load_dwordx4 s[8:11], s[0:1], 0x248
	s_load_dwordx2 s[14:15], s[0:1], 0x270
	s_lshl_b32 s16, s28, 2
	v_readlane_b32 s1, v255, 27
	s_mul_hi_u32 s1, s16, s1
	v_readlane_b32 s5, v255, 28
	s_mul_i32 s1, s1, s5
	s_sub_i32 s1, s16, s1
	s_sub_i32 s4, s1, s5
	s_cmp_ge_u32 s1, s5
	s_cselect_b32 s1, s4, s1
	s_sub_i32 s4, s1, s5
	s_cmp_ge_u32 s1, s5
	s_cselect_b32 s1, s4, s1
	s_mov_b32 s29, s2
	s_mov_b32 s0, s2
	s_cmp_eq_u32 s1, 0
	s_cselect_b64 s[4:5], -1, 0
	s_cmp_lt_i32 s0, s1
	s_cselect_b64 s[6:7], -1, 0
	s_or_b64 s[4:5], s[4:5], s[6:7]
	s_and_b64 vcc, exec, s[4:5]
	s_branch .LBB0_1310
	s_sub_i32 s0, s0, s1
	s_and_b32 s0, s0, 3
	s_mul_i32 s6, s0, 0x20d0
	s_memrealtime s[0:1]
	s_memrealtime s[4:5]
	s_addk_i32 s6, 0x20d0
	s_waitcnt lgkmcnt(0)
	s_and_b32 s1, s6, 0xfff0
	s_mul_i32 s1, s1, 0xcccd
	s_lshr_b32 s1, s1, 20
	s_sub_i32 s4, s4, s0
	s_cmp_le_u32 s1, s4
	s_cbranch_scc1 .LBB0_1310
